# pre-flush variant: arrivals 1 and 17 of each XCD issue the early L2 write-back
# speedup vs baseline: 1.0026x; 1.0000x over previous
.Ldvd_19:
	v_add_u32_e32 v6, 1, v5
	v_mad_u64_u32 v[4:5], s[2:3], v4, v3, v[4:5]
	v_cmp_ne_u32_e32 vcc, v6, v4
	s_and_saveexec_b64 s[2:3], vcc
	s_xor_b64 s[2:3], exec, s[2:3]
	v_readlane_b32 s37, v253, 9
	s_cbranch_execz .LBB0_223
	s_waitcnt lgkmcnt(0)
	v_and_b32_e32 v7, 15, v6
	v_cmp_eq_u32_e32 vcc, 1, v7
	s_cbranch_vccz .Lpf_9
	buffer_wbl2 sc1

.Ldvd_15:
	v_add_u32_e32 v6, 1, v5
	v_mad_u64_u32 v[4:5], s[2:3], v4, v3, v[4:5]
	v_cmp_ne_u32_e32 vcc, v6, v4
	s_and_saveexec_b64 s[2:3], vcc
	s_xor_b64 s[2:3], exec, s[2:3]
	v_readlane_b32 s37, v253, 9
	s_cbranch_execz .LBB0_454
	s_waitcnt lgkmcnt(0)
	v_and_b32_e32 v7, 15, v6
	v_cmp_eq_u32_e32 vcc, 1, v7
	s_cbranch_vccz .Lpf_7
	v_cmp_eq_u32_e32 vcc, 0, v20
	s_cbranch_vccnz .Lpf_7
	buffer_wbl2 sc1

.Ldvd_7:
	v_add_u32_e32 v6, 1, v5
	v_mad_u64_u32 v[4:5], s[2:3], v4, v3, v[4:5]
	v_cmp_ne_u32_e32 vcc, v6, v4
	s_and_saveexec_b64 s[2:3], vcc
	s_xor_b64 s[2:3], exec, s[2:3]
	s_cbranch_execz .LBB0_766
	s_waitcnt lgkmcnt(0)
	v_and_b32_e32 v7, 15, v6
	v_cmp_eq_u32_e32 vcc, 1, v7
	s_cbranch_vccz .Lpf_3
	buffer_wbl2 sc1

.Ldvd_5:
	v_add_u32_e32 v6, 1, v5
	v_mad_u64_u32 v[4:5], s[2:3], v4, v3, v[4:5]
	v_cmp_ne_u32_e32 vcc, v6, v4
	s_and_saveexec_b64 s[2:3], vcc
	s_xor_b64 s[2:3], exec, s[2:3]
	s_cbranch_execz .LBB0_926
	s_waitcnt lgkmcnt(0)
	v_and_b32_e32 v7, 15, v6
	v_cmp_eq_u32_e32 vcc, 1, v7
	s_cbranch_vccz .Lpf_2
	v_cmp_eq_u32_e32 vcc, 0, v20
	s_cbranch_vccnz .Lpf_2
	buffer_wbl2 sc1
